# P7 SwiGLU epilogue trimmed 903->721 instr (merged exp2 constant, dropped no-op 448 guard, +1 folded into bias) on top of v2
# baseline (speedup 1.0000x reference)
.LBB0_783:
	v_and_b32_e32 v1, 48, v178
	v_lshlrev_b32_e32 v4, 2, v200
	v_lshl_or_b32 v2, s11, 6, v200
	v_lshl_or_b32 v3, v200, 6, v1
	s_lshl_b32 s11, s11, 13
	v_and_b32_e32 v4, 32, v4
	s_lshl_b32 s5, s5, 5
	v_bitop3_b32 v202, v3, s11, v4 bitop3:0xde
	s_and_b32 s5, s5, 0x60
	v_lshlrev_b32_e32 v3, 6, v178
	s_movk_i32 s11, 0x3c0
	v_and_or_b32 v1, v3, s11, v1
	s_lshl_b32 s11, s5, 7
	s_add_u32 s18, s6, 0x4000
	s_addc_u32 s19, s7, 0
	s_add_i32 s53, s46, 0x8000
	v_lshl_add_u64 v[4:5], s[18:19], 0, v[176:177]
	s_mov_b32 m0, s53
	s_add_i32 s54, s46, 0xa000
	s_waitcnt vmcnt(4)
	s_barrier
	global_load_lds_dwordx4 v[4:5], off
	v_lshl_add_u64 v[4:5], s[18:19], 0, v[180:181]
	s_add_u32 s18, s90, 0xd040080
	s_mov_b32 m0, s54
	s_addc_u32 s19, s91, 0
	global_load_lds_dwordx4 v[4:5], off
	s_add_i32 m0, s46, 0x18000
	v_lshl_add_u64 v[4:5], s[18:19], 0, v[182:183]
	global_load_lds_dwordx4 v[4:5], off
	s_add_i32 m0, s46, 0x1a000
	v_lshl_add_u64 v[4:5], s[18:19], 0, v[184:185]
	s_add_u32 s18, s6, 0x404000
	s_addc_u32 s19, s7, 0
	s_add_i32 s55, s46, 0xc000
	global_load_lds_dwordx4 v[4:5], off
	v_lshl_add_u64 v[4:5], s[18:19], 0, v[176:177]
	s_mov_b32 m0, s55
	s_add_i32 s56, s46, 0xe000
	global_load_lds_dwordx4 v[4:5], off
	v_lshl_add_u64 v[4:5], s[18:19], 0, v[180:181]
	s_mov_b32 m0, s56
	v_lshlrev_b32_e32 v3, 2, v178
	global_load_lds_dwordx4 v[4:5], off
	v_and_b32_e32 v3, 32, v3
	v_bitop3_b32 v6, s11, v1, v3 bitop3:0xf6
	v_mov_b32_e32 v1, v183
	v_lshl_add_u64 v[186:187], s[16:17], 0, v[0:1]
	s_ashr_i32 s17, s33, 31
	s_lshr_b32 s17, s17, 29
	s_add_i32 s17, s33, s17
	s_and_b32 s18, s17, -8
	s_ashr_i32 s16, s96, 3
	s_sub_i32 s18, s33, s18
	s_mul_i32 s16, s16, s18
	s_ashr_i32 s17, s17, 3
	s_add_i32 s18, s16, s17
	s_add_u32 s16, s90, s5
	s_addc_u32 s17, s91, 0
	s_and_b64 s[2:3], s[2:3], exec
	s_mov_b32 s2, 0x20944
	s_cselect_b32 s57, s18, s33
	s_add_i32 s58, s2, 0x100
	s_mov_b32 s2, 0x20948
	s_add_i32 s59, s2, 0x100
	s_mov_b32 s2, 0x2094c
	s_add_i32 s60, s2, 0x100
	s_mov_b32 s2, 0x20950
	s_add_i32 s61, s2, 0x100
	s_mov_b32 s2, 0x20954
	s_add_i32 s62, s2, 0x100
	s_mov_b32 s2, 0x20958
	s_add_i32 s63, s2, 0x100
	s_mov_b32 s2, 0x2095c
	s_add_i32 s64, s2, 0x100
	s_mov_b32 s2, 0x20960
	s_add_i32 s65, s2, 0x100
	s_mov_b32 s2, 0x20964
	s_add_i32 s68, s2, 0x100
	s_mov_b32 s2, 0x20968
	s_add_i32 s69, s2, 0x100
	s_mov_b32 s2, 0x2096c
	s_add_i32 s70, s2, 0x100
	s_mov_b32 s2, 0x20970
	s_addk_i32 s2, 0x100
	v_writelane_b32 v250, s2, 4
	s_mov_b32 s2, 0x20974
	s_addk_i32 s2, 0x100
	v_writelane_b32 v250, s2, 3
	s_mov_b32 s2, 0x20978
	s_addk_i32 s2, 0x100
	v_writelane_b32 v250, s2, 5
	s_mov_b32 s2, 0x2097c
	s_addk_i32 s2, 0x100
	v_writelane_b32 v250, s2, 6
	s_mov_b32 s2, 0x20980
	s_addk_i32 s2, 0x100
	v_writelane_b32 v250, s2, 7
	s_mov_b32 s2, 0x20984
	s_addk_i32 s2, 0x100
	v_writelane_b32 v250, s2, 8
	s_mov_b32 s2, 0x20988
	s_addk_i32 s2, 0x100
	v_writelane_b32 v250, s2, 9
	s_mov_b32 s2, 0x2098c
	s_addk_i32 s2, 0x100
	v_writelane_b32 v250, s2, 10
	s_mov_b32 s2, 0x20990
	s_addk_i32 s2, 0x100
	v_writelane_b32 v250, s2, 11
	s_mov_b32 s2, 0x20994
	s_addk_i32 s2, 0x100
	v_writelane_b32 v250, s2, 12
	s_mov_b32 s2, 0x20998
	s_addk_i32 s2, 0x100
	v_writelane_b32 v250, s2, 13
	s_mov_b32 s2, 0x2099c
	s_addk_i32 s2, 0x100
	v_writelane_b32 v250, s2, 14
	s_mov_b32 s2, 0x209a0
	s_addk_i32 s2, 0x100
	v_writelane_b32 v250, s2, 15
	s_mov_b32 s2, 0x209a4
	s_addk_i32 s2, 0x100
	v_writelane_b32 v250, s2, 16
	s_mov_b32 s2, 0x209a8
	s_addk_i32 s2, 0x100
	v_writelane_b32 v250, s2, 17
	s_mov_b32 s2, 0x209ac
	s_addk_i32 s2, 0x100
	v_writelane_b32 v250, s2, 18
	s_mov_b32 s2, 0x209b0
	s_addk_i32 s2, 0x100
	v_writelane_b32 v250, s2, 19
	s_mov_b32 s2, 0x209b4
	s_addk_i32 s2, 0x100
	v_writelane_b32 v250, s2, 20
	s_mov_b32 s2, 0x209b8
	s_addk_i32 s2, 0x100
	v_and_b32_e32 v4, 12, v218
	v_mov_b32_e32 v5, v183
	v_mov_b32_e32 v3, v183
	v_writelane_b32 v250, s2, 21
	s_mov_b32 s2, 0x209bc
	s_waitcnt vmcnt(6)
	v_lshlrev_b64 v[2:3], 7, v[2:3]
	v_lshl_add_u64 v[0:1], s[16:17], 0, v[4:5]
	s_addk_i32 s2, 0x100
	s_mov_b32 s11, 0x18000
	v_lshl_add_u64 v[0:1], v[0:1], 0, v[2:3]
	s_mov_b64 s[16:17], 0xf1a0000
	v_writelane_b32 v250, s2, 22
	s_mov_b32 s2, 0x14000
	v_lshl_add_u64 v[188:189], v[0:1], 0, s[16:17]
	v_mov_b32_e32 v203, 0x7f7f7f7f
	v_mov_b32_e32 v204, 0x79797979
	s_add_i32 s79, s2, 0x100
	s_mov_b64 s[16:17], 0x80
	s_lshl_b32 s73, s5, 2
	v_lshlrev_b32_e32 v194, 2, v4
	s_mov_b32 s80, 0xc0c00000
	s_mov_b32 s81, 0xc3e00000
	v_add_u32_e32 v205, 0x100, v6
	s_add_i32 s77, s11, 0x100
	v_mov_b32_e32 v206, 0x41000000
	v_mov_b32_e32 v207, 0x43e00000
	v_mov_b32_e32 v48, v183
	v_mov_b32_e32 v49, v183
	v_mov_b32_e32 v50, v183
	v_mov_b32_e32 v51, v183
	v_mov_b32_e32 v52, v183
	v_mov_b32_e32 v53, v183
	v_mov_b32_e32 v54, v183
	v_mov_b32_e32 v55, v183
	v_mov_b32_e32 v56, v183
	v_mov_b32_e32 v57, v183
	v_mov_b32_e32 v58, v183
	v_mov_b32_e32 v59, v183
	v_mov_b32_e32 v60, v183
	v_mov_b32_e32 v61, v183
	v_mov_b32_e32 v62, v183
	v_mov_b32_e32 v63, v183
	v_mov_b32_e32 v64, v183
	v_mov_b32_e32 v65, v183
	v_mov_b32_e32 v66, v183
	v_mov_b32_e32 v67, v183
	v_mov_b32_e32 v68, v183
	v_mov_b32_e32 v69, v183
	v_mov_b32_e32 v70, v183
	v_mov_b32_e32 v71, v183
	v_mov_b32_e32 v72, v183
	v_mov_b32_e32 v73, v183
	v_mov_b32_e32 v74, v183
	v_mov_b32_e32 v75, v183
	v_mov_b32_e32 v76, v183
	v_mov_b32_e32 v77, v183
	v_mov_b32_e32 v78, v183
	v_mov_b32_e32 v79, v183
	v_mov_b32_e32 v80, v183
	v_mov_b32_e32 v81, v183
	v_mov_b32_e32 v82, v183
	v_mov_b32_e32 v83, v183
	v_mov_b32_e32 v84, v183
	v_mov_b32_e32 v85, v183
	v_mov_b32_e32 v86, v183
	v_mov_b32_e32 v87, v183
	v_mov_b32_e32 v88, v183
	v_mov_b32_e32 v89, v183
	v_mov_b32_e32 v90, v183
	v_mov_b32_e32 v91, v183
	v_mov_b32_e32 v92, v183
	v_mov_b32_e32 v93, v183
	v_mov_b32_e32 v94, v183
	v_mov_b32_e32 v95, v183
	v_mov_b32_e32 v96, v183
	v_mov_b32_e32 v97, v183
	v_mov_b32_e32 v98, v183
	v_mov_b32_e32 v99, v183
	v_mov_b32_e32 v100, v183
	v_mov_b32_e32 v101, v183
	v_mov_b32_e32 v102, v183
	v_mov_b32_e32 v103, v183
	v_mov_b32_e32 v104, v183
	v_mov_b32_e32 v105, v183
	v_mov_b32_e32 v106, v183
	v_mov_b32_e32 v107, v183
	v_mov_b32_e32 v108, v183
	v_mov_b32_e32 v109, v183
	v_mov_b32_e32 v110, v183
	v_mov_b32_e32 v111, v183
	v_mov_b32_e32 v112, v183
	v_mov_b32_e32 v113, v183
	v_mov_b32_e32 v114, v183
	v_mov_b32_e32 v115, v183
	v_mov_b32_e32 v116, v183
	v_mov_b32_e32 v117, v183
	v_mov_b32_e32 v118, v183
	v_mov_b32_e32 v119, v183
	v_mov_b32_e32 v120, v183
	v_mov_b32_e32 v121, v183
	v_mov_b32_e32 v122, v183
	v_mov_b32_e32 v123, v183
	v_mov_b32_e32 v124, v183
	v_mov_b32_e32 v125, v183
	v_mov_b32_e32 v126, v183
	v_mov_b32_e32 v127, v183
	v_mov_b32_e32 v128, v183
	v_mov_b32_e32 v129, v183
	v_mov_b32_e32 v130, v183
	v_mov_b32_e32 v131, v183
	v_mov_b32_e32 v132, v183
	v_mov_b32_e32 v133, v183
	v_mov_b32_e32 v134, v183
	v_mov_b32_e32 v135, v183
	v_mov_b32_e32 v136, v183
	v_mov_b32_e32 v137, v183
	v_mov_b32_e32 v138, v183
	v_mov_b32_e32 v139, v183
	v_mov_b32_e32 v140, v183
	v_mov_b32_e32 v141, v183
	v_mov_b32_e32 v142, v183
	v_mov_b32_e32 v143, v183
	v_mov_b32_e32 v144, v183
	v_mov_b32_e32 v145, v183
	v_mov_b32_e32 v146, v183
	v_mov_b32_e32 v147, v183
	v_mov_b32_e32 v148, v183
	v_mov_b32_e32 v149, v183
	v_mov_b32_e32 v150, v183
	v_mov_b32_e32 v151, v183
	v_mov_b32_e32 v152, v183
	v_mov_b32_e32 v153, v183
	v_mov_b32_e32 v154, v183
	v_mov_b32_e32 v155, v183
	v_mov_b32_e32 v156, v183
	v_mov_b32_e32 v157, v183
	v_mov_b32_e32 v158, v183
	v_mov_b32_e32 v159, v183
	v_mov_b32_e32 v160, v183
	v_mov_b32_e32 v161, v183
	v_mov_b32_e32 v162, v183
	v_mov_b32_e32 v163, v183
	v_mov_b32_e32 v164, v183
	v_mov_b32_e32 v165, v183
	v_mov_b32_e32 v166, v183
	v_mov_b32_e32 v167, v183
	v_mov_b32_e32 v168, v183
	v_mov_b32_e32 v169, v183
	v_mov_b32_e32 v170, v183
	v_mov_b32_e32 v171, v183
	v_mov_b32_e32 v172, v183
	v_mov_b32_e32 v173, v183
	v_mov_b32_e32 v174, v183
	v_mov_b32_e32 v175, v183
	s_barrier
	s_branch .LBB0_785

.LBB0_827:
	s_ashr_i32 s5, s4, 31
	s_lshl_b64 s[26:27], s[4:5], 14
	s_add_u32 s5, s82, s26
	s_addc_u32 s23, s83, s27
	s_ashr_i32 s11, s10, 31
	s_lshl_b64 s[26:27], s[10:11], 2
	s_add_u32 s5, s5, s26
	s_addc_u32 s11, s23, s27
	s_add_u32 s26, s5, s73
	s_addc_u32 s27, s11, 0
	global_load_dwordx4 v[8:11], v194, s[26:27]
	global_load_dwordx4 v[4:7], v194, s[26:27] offset:64
	v_mov_b32_e32 v195, v183
	v_lshl_add_u64 v[0:1], s[26:27], 0, v[194:195]
	s_movk_i32 s5, 0x2000
	v_add_co_u32_e32 v0, vcc, s5, v0
	v_mov_b32_e32 v18, v183
	s_nop 0
	v_addc_co_u32_e32 v1, vcc, 0, v1, vcc
	global_load_dwordx4 v[12:15], v[0:1], off
	s_nop 0
	global_load_dwordx4 v[0:3], v[0:1], off offset:64
	s_ashr_i32 s5, s45, 3
	s_ashr_i32 s11, s10, 7
	s_and_b32 s5, s5, -16
	s_add_i32 s26, s5, s11
	s_ashr_i32 s27, s26, 31
	s_lshl_b64 s[26:27], s[26:27], 14
	v_lshl_add_u64 v[16:17], v[188:189], 0, s[26:27]
	s_movk_i32 s5, 0x1000
	s_mov_b64 s[26:27], 0x40000
	s_waitcnt vmcnt(0)
	v_add_f32_e32 v12, 1.0, v12
	v_add_f32_e32 v13, 1.0, v13
	v_add_f32_e32 v14, 1.0, v14
	v_add_f32_e32 v15, 1.0, v15
	v_add_f32_e32 v0, 1.0, v0
	v_add_f32_e32 v1, 1.0, v1
	v_add_f32_e32 v2, 1.0, v2
	v_add_f32_e32 v3, 1.0, v3
	v_add_f32_e32 v19, v172, v8
	v_add_f32_e32 v20, v173, v9
	v_min_f32_e32 v19, 0x40e00000, v19
	v_min_f32_e32 v20, 0x40e00000, v20
	v_mul_f32_e32 v27, 0xc01d265f, v19
	v_mul_f32_e32 v29, 0xc01d265f, v20
	v_add_f32_e32 v21, v174, v10
	v_add_f32_e32 v22, v175, v11
	v_exp_f32_e32 v27, v27
	v_exp_f32_e32 v29, v29
	v_min_f32_e32 v21, 0x40e00000, v21
	v_min_f32_e32 v22, 0x40e00000, v22
	v_mul_f32_e32 v31, 0xc01d265f, v21
	v_mul_f32_e32 v33, 0xc01d265f, v22
	v_add_f32_e32 v23, v168, v4
	v_min_f32_e32 v23, 0x40e00000, v23
	v_exp_f32_e32 v31, v31
	v_exp_f32_e32 v33, v33
	v_add_f32_e32 v27, 1.0, v27
	v_add_f32_e32 v29, 1.0, v29
	v_mul_f32_e32 v35, 0xc01d265f, v23
	v_rcp_f32_e32 v27, v27
	v_rcp_f32_e32 v29, v29
	v_add_f32_e32 v26, v140, v12
	v_add_f32_e32 v28, v141, v13
	v_exp_f32_e32 v35, v35
	v_med3_f32 v26, v26, s80, v206
	v_med3_f32 v28, v28, s80, v206
	v_add_f32_e32 v31, 1.0, v31
	v_add_f32_e32 v33, 1.0, v33
	v_add_f32_e32 v25, v170, v6
	v_rcp_f32_e32 v31, v31
	v_rcp_f32_e32 v33, v33
	v_mul_f32_e32 v19, v19, v27
	v_mul_f32_e32 v20, v20, v29
	v_min_f32_e32 v25, 0x40e00000, v25
	v_mul_f32_e32 v19, v26, v19
	v_mul_f32_e32 v20, v28, v20
	v_add_f32_e32 v30, v142, v14
	v_add_f32_e32 v32, v143, v15
	v_mul_f32_e32 v38, 0xc01d265f, v25
	v_add_f32_e32 v35, 1.0, v35
	v_med3_f32 v30, v30, s80, v206
	v_med3_f32 v32, v32, s80, v206
	v_rcp_f32_e32 v35, v35
	v_cvt_pk_fp8_f32 v18, v19, v20
	v_add_f32_e32 v24, v169, v5
	v_exp_f32_e32 v38, v38
	v_mul_f32_e32 v21, v21, v31
	v_mul_f32_e32 v22, v22, v33
	v_min_f32_e32 v24, 0x40e00000, v24
	v_add_f32_e32 v34, v136, v0
	v_mul_f32_e32 v21, v30, v21
	v_mul_f32_e32 v22, v32, v22
	v_mul_f32_e32 v37, 0xc01d265f, v24
	v_med3_f32 v34, v34, s80, v206
	v_mov_b32_e32 v20, v21
	v_mov_b32_e32 v21, v22
	v_add_f32_e32 v22, v171, v7
	v_mul_f32_e32 v23, v23, v35
	v_cvt_pk_fp8_f32 v18, v20, v21 op_sel:[0,0,1]
	v_min_f32_e32 v22, 0x40e00000, v22
	v_exp_f32_e32 v37, v37
	v_mul_f32_e32 v19, v34, v23
	v_add_f32_e32 v21, 1.0, v38
	v_mul_f32_e32 v23, 0xc01d265f, v22
	v_rcp_f32_e32 v21, v21
	v_exp_f32_e32 v23, v23
	global_store_dword v[16:17], v18, off
	v_add_f32_e32 v18, v138, v2
	v_add_f32_e32 v37, 1.0, v37
	v_med3_f32 v18, v18, s80, v206
	v_rcp_f32_e32 v37, v37
	v_mul_f32_e32 v21, v25, v21
	v_mul_f32_e32 v18, v18, v21
	v_add_f32_e32 v21, 1.0, v23
	v_add_f32_e32 v36, v137, v1
	v_rcp_f32_e32 v21, v21
	v_med3_f32 v36, v36, s80, v206
	v_mul_f32_e32 v24, v24, v37
	v_mul_f32_e32 v20, v36, v24
	v_add_f32_e32 v23, v139, v3
	v_mul_f32_e32 v21, v22, v21
	v_mov_b32_e32 v22, v183
	v_cvt_pk_fp8_f32 v22, v19, v20
	v_med3_f32 v19, v23, s80, v206
	v_mul_f32_e32 v19, v19, v21
	v_cvt_pk_fp8_f32 v22, v18, v19 op_sel:[0,0,1]
	v_add_f32_e32 v18, v164, v8
	v_min_f32_e32 v18, 0x40e00000, v18
	v_mul_f32_e32 v19, 0xc01d265f, v18
	v_exp_f32_e32 v19, v19
	v_add_f32_e32 v21, v165, v9
	v_min_f32_e32 v21, 0x40e00000, v21
	global_store_dword v[16:17], v22, off offset:16
	v_add_f32_e32 v19, 1.0, v19
	v_mul_f32_e32 v22, 0xc01d265f, v21
	v_rcp_f32_e32 v19, v19
	v_exp_f32_e32 v22, v22
	v_add_f32_e32 v20, v132, v12
	v_mul_f32_e32 v18, v18, v19
	v_med3_f32 v19, v20, s80, v206
	v_mul_f32_e32 v18, v19, v18
	v_add_f32_e32 v19, 1.0, v22
	v_rcp_f32_e32 v19, v19
	v_add_f32_e32 v20, v133, v13
	v_med3_f32 v20, v20, s80, v206
	v_mul_f32_e32 v19, v21, v19
	v_mul_f32_e32 v19, v20, v19
	v_add_f32_e32 v20, v166, v10
	v_min_f32_e32 v20, 0x40e00000, v20
	v_mul_f32_e32 v21, 0xc01d265f, v20
	v_exp_f32_e32 v21, v21
	v_add_f32_e32 v23, v167, v11
	v_min_f32_e32 v23, 0x40e00000, v23
	v_mul_f32_e32 v24, 0xc01d265f, v23
	v_add_f32_e32 v21, 1.0, v21
	v_rcp_f32_e32 v21, v21
	v_exp_f32_e32 v24, v24
	v_add_f32_e32 v22, v134, v14
	v_mul_f32_e32 v20, v20, v21
	v_med3_f32 v21, v22, s80, v206
	v_mul_f32_e32 v20, v21, v20
	v_add_f32_e32 v21, 1.0, v24
	v_rcp_f32_e32 v21, v21
	v_add_f32_e32 v22, v135, v15
	v_mul_f32_e32 v21, v23, v21
	v_mov_b32_e32 v23, v183
	v_cvt_pk_fp8_f32 v23, v18, v19
	v_med3_f32 v18, v22, s80, v206
	v_mul_f32_e32 v18, v18, v21
	v_cvt_pk_fp8_f32 v23, v20, v18 op_sel:[0,0,1]
	v_add_f32_e32 v18, v160, v4
	v_min_f32_e32 v18, 0x40e00000, v18
	v_mul_f32_e32 v19, 0xc01d265f, v18
	v_exp_f32_e32 v19, v19
	v_add_f32_e32 v21, v161, v5
	v_min_f32_e32 v21, 0x40e00000, v21
	v_mul_f32_e32 v22, 0xc01d265f, v21
	v_add_f32_e32 v19, 1.0, v19
	v_rcp_f32_e32 v19, v19
	v_exp_f32_e32 v22, v22
	v_add_f32_e32 v20, v128, v0
	v_mul_f32_e32 v18, v18, v19
	v_med3_f32 v19, v20, s80, v206
	v_mul_f32_e32 v18, v19, v18
	v_add_f32_e32 v19, 1.0, v22
	v_rcp_f32_e32 v19, v19
	v_add_f32_e32 v20, v129, v1
	v_med3_f32 v20, v20, s80, v206
	v_mul_f32_e32 v19, v21, v19
	v_mul_f32_e32 v19, v20, v19
	v_add_f32_e32 v20, v162, v6
	v_min_f32_e32 v20, 0x40e00000, v20
	v_mul_f32_e32 v21, 0xc01d265f, v20
	v_exp_f32_e32 v21, v21
	global_store_dword v[16:17], v23, off offset:2048
	v_add_f32_e32 v23, v163, v7
	v_min_f32_e32 v23, 0x40e00000, v23
	v_add_f32_e32 v21, 1.0, v21
	v_mul_f32_e32 v24, 0xc01d265f, v23
	v_rcp_f32_e32 v21, v21
	v_exp_f32_e32 v24, v24
	v_add_f32_e32 v22, v130, v2
	v_mul_f32_e32 v20, v20, v21
	v_med3_f32 v21, v22, s80, v206
	v_mul_f32_e32 v20, v21, v20
	v_add_f32_e32 v21, 1.0, v24
	v_rcp_f32_e32 v21, v21
	v_add_f32_e32 v22, v131, v3
	v_mul_f32_e32 v21, v23, v21
	v_mov_b32_e32 v23, v183
	v_cvt_pk_fp8_f32 v23, v18, v19
	v_med3_f32 v18, v22, s80, v206
	v_mul_f32_e32 v18, v18, v21
	v_cvt_pk_fp8_f32 v23, v20, v18 op_sel:[0,0,1]
	v_add_f32_e32 v18, v156, v8
	v_min_f32_e32 v18, 0x40e00000, v18
	v_mul_f32_e32 v19, 0xc01d265f, v18
	v_exp_f32_e32 v19, v19
	v_add_f32_e32 v21, v157, v9
	v_min_f32_e32 v21, 0x40e00000, v21
	v_mul_f32_e32 v22, 0xc01d265f, v21
	v_add_f32_e32 v19, 1.0, v19
	v_rcp_f32_e32 v19, v19
	v_exp_f32_e32 v22, v22
	v_add_f32_e32 v20, v124, v12
	v_mul_f32_e32 v18, v18, v19
	v_med3_f32 v19, v20, s80, v206
	v_mul_f32_e32 v18, v19, v18
	v_add_f32_e32 v19, 1.0, v22
	v_rcp_f32_e32 v19, v19
	v_add_f32_e32 v20, v125, v13
	v_med3_f32 v20, v20, s80, v206
	v_mul_f32_e32 v19, v21, v19
	v_mul_f32_e32 v19, v20, v19
	v_add_f32_e32 v20, v158, v10
	v_min_f32_e32 v20, 0x40e00000, v20
	v_mul_f32_e32 v21, 0xc01d265f, v20
	v_exp_f32_e32 v21, v21
	global_store_dword v[16:17], v23, off offset:2064
	v_add_f32_e32 v23, v159, v11
	v_min_f32_e32 v23, 0x40e00000, v23
	v_add_f32_e32 v21, 1.0, v21
	v_mul_f32_e32 v24, 0xc01d265f, v23
	v_rcp_f32_e32 v21, v21
	v_exp_f32_e32 v24, v24
	v_add_f32_e32 v22, v126, v14
	v_mul_f32_e32 v20, v20, v21
	v_med3_f32 v21, v22, s80, v206
	v_mul_f32_e32 v20, v21, v20
	v_add_f32_e32 v21, 1.0, v24
	v_rcp_f32_e32 v21, v21
	v_add_f32_e32 v22, v127, v15
	v_mul_f32_e32 v21, v23, v21
	v_mov_b32_e32 v23, v183
	v_cvt_pk_fp8_f32 v23, v18, v19
	v_med3_f32 v18, v22, s80, v206
	v_mul_f32_e32 v18, v18, v21
	v_cvt_pk_fp8_f32 v23, v20, v18 op_sel:[0,0,1]
	v_add_f32_e32 v18, v152, v4
	v_min_f32_e32 v20, 0x40e00000, v18
	v_mul_f32_e32 v18, 0xc01d265f, v20
	v_exp_f32_e32 v21, v18
	v_add_f32_e32 v24, v153, v5
	v_min_f32_e32 v24, 0x40e00000, v24
	v_mul_f32_e32 v25, 0xc01d265f, v24
	v_add_f32_e32 v21, 1.0, v21
	v_rcp_f32_e32 v21, v21
	v_exp_f32_e32 v25, v25
	v_add_f32_e32 v22, v120, v0
	v_mul_f32_e32 v20, v20, v21
	v_med3_f32 v21, v22, s80, v206
	v_mul_f32_e32 v20, v21, v20
	v_add_f32_e32 v21, 1.0, v25
	v_rcp_f32_e32 v21, v21
	v_add_f32_e32 v22, v121, v1
	v_med3_f32 v22, v22, s80, v206
	v_mul_f32_e32 v21, v24, v21
	v_mul_f32_e32 v21, v22, v21
	v_add_f32_e32 v22, v154, v6
	v_min_f32_e32 v22, 0x40e00000, v22
	v_mul_f32_e32 v24, 0xc01d265f, v22
	v_exp_f32_e32 v24, v24
	v_add_f32_e32 v26, v155, v7
	v_min_f32_e32 v26, 0x40e00000, v26
	v_mul_f32_e32 v27, 0xc01d265f, v26
	v_add_f32_e32 v24, 1.0, v24
	v_rcp_f32_e32 v24, v24
	v_exp_f32_e32 v27, v27
	v_add_f32_e32 v25, v122, v2
	v_mul_f32_e32 v22, v22, v24
	v_med3_f32 v24, v25, s80, v206
	v_mul_f32_e32 v22, v24, v22
	v_add_f32_e32 v24, 1.0, v27
	v_rcp_f32_e32 v24, v24
	v_add_f32_e32 v25, v123, v3
	v_med3_f32 v25, v25, s80, v206
	v_mul_f32_e32 v24, v26, v24
	v_mul_f32_e32 v24, v25, v24
	v_mov_b32_e32 v25, v183
	v_cvt_pk_fp8_f32 v25, v20, v21
	v_add_f32_e32 v20, v148, v8
	v_min_f32_e32 v20, 0x40e00000, v20
	v_mul_f32_e32 v21, 0xc01d265f, v20
	v_exp_f32_e32 v21, v21
	v_cvt_pk_fp8_f32 v25, v22, v24 op_sel:[0,0,1]
	v_add_f32_e32 v24, v149, v9
	v_min_f32_e32 v24, 0x40e00000, v24
	v_add_f32_e32 v21, 1.0, v21
	v_mul_f32_e32 v26, 0xc01d265f, v24
	v_rcp_f32_e32 v21, v21
	v_exp_f32_e32 v26, v26
	v_add_f32_e32 v22, v116, v12
	v_mul_f32_e32 v20, v20, v21
	v_med3_f32 v21, v22, s80, v206
	v_mul_f32_e32 v20, v21, v20
	v_add_f32_e32 v21, 1.0, v26
	v_rcp_f32_e32 v21, v21
	v_add_f32_e32 v22, v117, v13
	v_med3_f32 v22, v22, s80, v206
	v_mul_f32_e32 v21, v24, v21
	v_mul_f32_e32 v21, v22, v21
	v_add_f32_e32 v22, v150, v10
	v_min_f32_e32 v22, 0x40e00000, v22
	v_mul_f32_e32 v24, 0xc01d265f, v22
	v_exp_f32_e32 v24, v24
	v_add_f32_e32 v27, v151, v11
	v_min_f32_e32 v27, 0x40e00000, v27
	v_mul_f32_e32 v28, 0xc01d265f, v27
	v_add_f32_e32 v24, 1.0, v24
	v_rcp_f32_e32 v24, v24
	v_exp_f32_e32 v28, v28
	v_add_f32_e32 v26, v118, v14
	v_mul_f32_e32 v22, v22, v24
	v_med3_f32 v24, v26, s80, v206
	v_mul_f32_e32 v22, v24, v22
	v_add_f32_e32 v24, 1.0, v28
	v_rcp_f32_e32 v24, v24
	v_add_f32_e32 v26, v119, v15
	v_med3_f32 v26, v26, s80, v206
	v_mul_f32_e32 v24, v27, v24
	v_mul_f32_e32 v24, v26, v24
	v_mov_b32_e32 v26, v183
	v_cvt_pk_fp8_f32 v26, v20, v21
	v_add_f32_e32 v20, v144, v4
	v_min_f32_e32 v20, 0x40e00000, v20
	v_mul_f32_e32 v21, 0xc01d265f, v20
	v_exp_f32_e32 v21, v21
	v_cvt_pk_fp8_f32 v26, v22, v24 op_sel:[0,0,1]
	v_add_f32_e32 v24, v145, v5
	v_min_f32_e32 v24, 0x40e00000, v24
	v_add_f32_e32 v21, 1.0, v21
	v_mul_f32_e32 v27, 0xc01d265f, v24
	v_rcp_f32_e32 v21, v21
	v_exp_f32_e32 v27, v27
	v_add_f32_e32 v22, v112, v0
	v_mul_f32_e32 v20, v20, v21
	v_med3_f32 v21, v22, s80, v206
	v_mul_f32_e32 v20, v21, v20
	v_add_f32_e32 v21, 1.0, v27
	v_rcp_f32_e32 v21, v21
	v_add_f32_e32 v22, v113, v1
	v_med3_f32 v22, v22, s80, v206
	v_mul_f32_e32 v21, v24, v21
	v_mul_f32_e32 v21, v22, v21
	v_add_f32_e32 v22, v146, v6
	v_min_f32_e32 v22, 0x40e00000, v22
	v_mul_f32_e32 v24, 0xc01d265f, v22
	v_exp_f32_e32 v24, v24
	v_add_f32_e32 v28, v147, v7
	v_min_f32_e32 v28, 0x40e00000, v28
	v_mul_f32_e32 v29, 0xc01d265f, v28
	v_add_f32_e32 v24, 1.0, v24
	v_rcp_f32_e32 v24, v24
	v_exp_f32_e32 v29, v29
	v_add_f32_e32 v27, v114, v2
	v_mul_f32_e32 v22, v22, v24
	v_med3_f32 v24, v27, s80, v206
	v_mul_f32_e32 v22, v24, v22
	v_add_f32_e32 v24, 1.0, v29
	v_rcp_f32_e32 v24, v24
	v_add_f32_e32 v27, v115, v3
	v_mul_f32_e32 v24, v28, v24
	v_mov_b32_e32 v28, v183
	v_cvt_pk_fp8_f32 v28, v20, v21
	v_med3_f32 v20, v27, s80, v206
	v_mul_f32_e32 v20, v20, v24
	v_add_co_u32_e32 v18, vcc, s5, v16
	v_addc_co_u32_e32 v19, vcc, 0, v17, vcc
	v_cvt_pk_fp8_f32 v28, v22, v20 op_sel:[0,0,1]
	global_store_dword v[18:19], v23, off
	global_store_dword v[18:19], v25, off offset:16
	global_store_dword v[18:19], v26, off offset:2048
	global_store_dword v[18:19], v28, off offset:2064
	v_add_f32_e32 v18, v108, v8
	v_min_f32_e32 v20, 0x40e00000, v18
	v_mul_f32_e32 v18, 0xc01d265f, v20
	v_exp_f32_e32 v21, v18
	v_add_f32_e32 v23, v109, v9
	v_min_f32_e32 v23, 0x40e00000, v23
	v_mul_f32_e32 v24, 0xc01d265f, v23
	v_add_f32_e32 v21, 1.0, v21
	v_rcp_f32_e32 v21, v21
	v_exp_f32_e32 v24, v24
	v_add_f32_e32 v22, v76, v12
	v_mul_f32_e32 v20, v20, v21
	v_med3_f32 v21, v22, s80, v206
	v_mul_f32_e32 v20, v21, v20
	v_add_f32_e32 v21, 1.0, v24
	v_rcp_f32_e32 v21, v21
	v_add_f32_e32 v22, v77, v13
	v_med3_f32 v22, v22, s80, v206
	v_mul_f32_e32 v21, v23, v21
	v_mul_f32_e32 v21, v22, v21
	v_add_f32_e32 v22, v110, v10
	v_min_f32_e32 v22, 0x40e00000, v22
	v_mul_f32_e32 v23, 0xc01d265f, v22
	v_exp_f32_e32 v23, v23
	v_add_f32_e32 v25, v111, v11
	v_min_f32_e32 v25, 0x40e00000, v25
	v_mul_f32_e32 v26, 0xc01d265f, v25
	v_add_f32_e32 v23, 1.0, v23
	v_rcp_f32_e32 v23, v23
	v_exp_f32_e32 v26, v26
	v_add_f32_e32 v24, v78, v14
	v_mul_f32_e32 v22, v22, v23
	v_med3_f32 v23, v24, s80, v206
	v_mul_f32_e32 v22, v23, v22
	v_add_f32_e32 v23, 1.0, v26
	v_rcp_f32_e32 v23, v23
	v_add_f32_e32 v24, v79, v15
	v_mul_f32_e32 v23, v25, v23
	v_mov_b32_e32 v25, v183
	v_cvt_pk_fp8_f32 v25, v20, v21
	v_med3_f32 v20, v24, s80, v206
	v_mul_f32_e32 v20, v20, v23
	v_cvt_pk_fp8_f32 v25, v22, v20 op_sel:[0,0,1]
	v_add_f32_e32 v20, v104, v4
	v_min_f32_e32 v20, 0x40e00000, v20
	v_mul_f32_e32 v21, 0xc01d265f, v20
	v_exp_f32_e32 v21, v21
	v_add_f32_e32 v23, v105, v5
	v_min_f32_e32 v23, 0x40e00000, v23
	v_mul_f32_e32 v24, 0xc01d265f, v23
	v_add_f32_e32 v21, 1.0, v21
	v_rcp_f32_e32 v21, v21
	v_exp_f32_e32 v24, v24
	v_add_f32_e32 v22, v72, v0
	v_mul_f32_e32 v20, v20, v21
	v_med3_f32 v21, v22, s80, v206
	v_mul_f32_e32 v20, v21, v20
	v_add_f32_e32 v21, 1.0, v24
	v_rcp_f32_e32 v21, v21
	v_add_f32_e32 v22, v73, v1
	v_med3_f32 v22, v22, s80, v206
	v_mul_f32_e32 v21, v23, v21
	v_mul_f32_e32 v21, v22, v21
	v_add_f32_e32 v22, v106, v6
	v_min_f32_e32 v22, 0x40e00000, v22
	v_mul_f32_e32 v23, 0xc01d265f, v22
	s_mov_b32 s5, 0x41000
	v_lshl_add_u64 v[18:19], v[16:17], 0, s[26:27]
	v_add_co_u32_e32 v16, vcc, s5, v16
	v_exp_f32_e32 v23, v23
	s_nop 0
	v_addc_co_u32_e32 v17, vcc, 0, v17, vcc
	global_store_dword v[16:17], v25, off offset:-4096
	v_add_f32_e32 v25, v107, v7
	v_min_f32_e32 v25, 0x40e00000, v25
	v_add_f32_e32 v23, 1.0, v23
	v_mul_f32_e32 v26, 0xc01d265f, v25
	v_rcp_f32_e32 v23, v23
	v_exp_f32_e32 v26, v26
	v_add_f32_e32 v24, v74, v2
	v_mul_f32_e32 v22, v22, v23
	v_med3_f32 v23, v24, s80, v206
	v_mul_f32_e32 v22, v23, v22
	v_add_f32_e32 v23, 1.0, v26
	v_rcp_f32_e32 v23, v23
	v_add_f32_e32 v24, v75, v3
	v_mul_f32_e32 v23, v25, v23
	v_mov_b32_e32 v25, v183
	v_cvt_pk_fp8_f32 v25, v20, v21
	v_med3_f32 v20, v24, s80, v206
	v_mul_f32_e32 v20, v20, v23
	v_cvt_pk_fp8_f32 v25, v22, v20 op_sel:[0,0,1]
	v_add_f32_e32 v20, v100, v8
	v_min_f32_e32 v20, 0x40e00000, v20
	v_mul_f32_e32 v21, 0xc01d265f, v20
	v_exp_f32_e32 v21, v21
	v_add_f32_e32 v23, v101, v9
	v_min_f32_e32 v23, 0x40e00000, v23
	v_mul_f32_e32 v24, 0xc01d265f, v23
	v_add_f32_e32 v21, 1.0, v21
	v_rcp_f32_e32 v21, v21
	v_exp_f32_e32 v24, v24
	v_add_f32_e32 v22, v68, v12
	v_mul_f32_e32 v20, v20, v21
	v_med3_f32 v21, v22, s80, v206
	v_mul_f32_e32 v20, v21, v20
	v_add_f32_e32 v21, 1.0, v24
	v_rcp_f32_e32 v21, v21
	v_add_f32_e32 v22, v69, v13
	v_med3_f32 v22, v22, s80, v206
	v_mul_f32_e32 v21, v23, v21
	v_mul_f32_e32 v21, v22, v21
	v_add_f32_e32 v22, v102, v10
	v_min_f32_e32 v22, 0x40e00000, v22
	v_mul_f32_e32 v23, 0xc01d265f, v22
	v_exp_f32_e32 v23, v23
	global_store_dword v[18:19], v25, off offset:16
	v_add_f32_e32 v25, v103, v11
	v_min_f32_e32 v25, 0x40e00000, v25
	v_add_f32_e32 v23, 1.0, v23
	v_mul_f32_e32 v26, 0xc01d265f, v25
	v_rcp_f32_e32 v23, v23
	v_exp_f32_e32 v26, v26
	v_add_f32_e32 v24, v70, v14
	v_mul_f32_e32 v22, v22, v23
	v_med3_f32 v23, v24, s80, v206
	v_mul_f32_e32 v22, v23, v22
	v_add_f32_e32 v23, 1.0, v26
	v_rcp_f32_e32 v23, v23
	v_add_f32_e32 v24, v71, v15
	v_mul_f32_e32 v23, v25, v23
	v_mov_b32_e32 v25, v183
	v_cvt_pk_fp8_f32 v25, v20, v21
	v_med3_f32 v20, v24, s80, v206
	v_mul_f32_e32 v20, v20, v23
	v_cvt_pk_fp8_f32 v25, v22, v20 op_sel:[0,0,1]
	v_add_f32_e32 v20, v96, v4
	v_min_f32_e32 v20, 0x40e00000, v20
	v_mul_f32_e32 v21, 0xc01d265f, v20
	v_exp_f32_e32 v21, v21
	v_add_f32_e32 v23, v97, v5
	v_min_f32_e32 v23, 0x40e00000, v23
	v_mul_f32_e32 v24, 0xc01d265f, v23
	v_add_f32_e32 v21, 1.0, v21
	v_rcp_f32_e32 v21, v21
	v_exp_f32_e32 v24, v24
	v_add_f32_e32 v22, v64, v0
	v_mul_f32_e32 v20, v20, v21
	v_med3_f32 v21, v22, s80, v206
	v_mul_f32_e32 v20, v21, v20
	v_add_f32_e32 v21, 1.0, v24
	v_rcp_f32_e32 v21, v21
	v_add_f32_e32 v22, v65, v1
	v_med3_f32 v22, v22, s80, v206
	v_mul_f32_e32 v21, v23, v21
	v_mul_f32_e32 v21, v22, v21
	v_add_f32_e32 v22, v98, v6
	v_min_f32_e32 v22, 0x40e00000, v22
	v_mul_f32_e32 v23, 0xc01d265f, v22
	v_exp_f32_e32 v23, v23
	global_store_dword v[18:19], v25, off offset:2048
	v_add_f32_e32 v25, v99, v7
	v_min_f32_e32 v25, 0x40e00000, v25
	v_add_f32_e32 v23, 1.0, v23
	v_mul_f32_e32 v26, 0xc01d265f, v25
	v_rcp_f32_e32 v23, v23
	v_exp_f32_e32 v26, v26
	v_add_f32_e32 v24, v66, v2
	v_mul_f32_e32 v22, v22, v23
	v_med3_f32 v23, v24, s80, v206
	v_mul_f32_e32 v22, v23, v22
	v_add_f32_e32 v23, 1.0, v26
	v_rcp_f32_e32 v23, v23
	v_add_f32_e32 v24, v67, v3
	v_mul_f32_e32 v23, v25, v23
	v_mov_b32_e32 v25, v183
	v_cvt_pk_fp8_f32 v25, v20, v21
	v_med3_f32 v20, v24, s80, v206
	v_mul_f32_e32 v20, v20, v23
	v_cvt_pk_fp8_f32 v25, v22, v20 op_sel:[0,0,1]
	v_add_f32_e32 v20, v92, v8
	v_min_f32_e32 v20, 0x40e00000, v20
	v_mul_f32_e32 v21, 0xc01d265f, v20
	v_exp_f32_e32 v21, v21
	global_store_dword v[18:19], v25, off offset:2064
	v_add_f32_e32 v18, v60, v12
	v_med3_f32 v18, v18, s80, v206
	v_add_f32_e32 v19, 1.0, v21
	v_add_f32_e32 v21, v93, v9
	v_min_f32_e32 v21, 0x40e00000, v21
	v_mul_f32_e32 v22, 0xc01d265f, v21
	v_rcp_f32_e32 v19, v19
	v_exp_f32_e32 v22, v22
	v_mul_f32_e32 v19, v20, v19
	v_mul_f32_e32 v18, v18, v19
	v_add_f32_e32 v19, 1.0, v22
	v_rcp_f32_e32 v19, v19
	v_add_f32_e32 v20, v61, v13
	v_med3_f32 v20, v20, s80, v206
	v_mul_f32_e32 v19, v21, v19
	v_mul_f32_e32 v19, v20, v19
	v_add_f32_e32 v20, v94, v10
	v_min_f32_e32 v20, 0x40e00000, v20
	v_mul_f32_e32 v21, 0xc01d265f, v20
	v_exp_f32_e32 v21, v21
	v_add_f32_e32 v23, v95, v11
	v_min_f32_e32 v23, 0x40e00000, v23
	v_mul_f32_e32 v24, 0xc01d265f, v23
	v_add_f32_e32 v21, 1.0, v21
	v_rcp_f32_e32 v21, v21
	v_exp_f32_e32 v24, v24
	v_add_f32_e32 v22, v62, v14
	v_mul_f32_e32 v20, v20, v21
	v_med3_f32 v21, v22, s80, v206
	v_mul_f32_e32 v20, v21, v20
	v_add_f32_e32 v21, 1.0, v24
	v_rcp_f32_e32 v21, v21
	v_add_f32_e32 v22, v63, v15
	v_mul_f32_e32 v21, v23, v21
	v_mov_b32_e32 v23, v183
	v_cvt_pk_fp8_f32 v23, v18, v19
	v_med3_f32 v18, v22, s80, v206
	v_mul_f32_e32 v18, v18, v21
	v_cvt_pk_fp8_f32 v23, v20, v18 op_sel:[0,0,1]
	v_add_f32_e32 v18, v88, v4
	v_min_f32_e32 v18, 0x40e00000, v18
	v_mul_f32_e32 v19, 0xc01d265f, v18
	v_exp_f32_e32 v19, v19
	v_add_f32_e32 v21, v89, v5
	v_min_f32_e32 v21, 0x40e00000, v21
	v_mul_f32_e32 v22, 0xc01d265f, v21
	v_add_f32_e32 v19, 1.0, v19
	v_rcp_f32_e32 v19, v19
	v_exp_f32_e32 v22, v22
	v_add_f32_e32 v20, v56, v0
	v_mul_f32_e32 v18, v18, v19
	v_med3_f32 v19, v20, s80, v206
	v_mul_f32_e32 v18, v19, v18
	v_add_f32_e32 v19, 1.0, v22
	v_rcp_f32_e32 v19, v19
	v_add_f32_e32 v20, v57, v1
	v_med3_f32 v20, v20, s80, v206
	v_mul_f32_e32 v19, v21, v19
	v_mul_f32_e32 v19, v20, v19
	v_add_f32_e32 v20, v90, v6
	v_min_f32_e32 v20, 0x40e00000, v20
	v_mul_f32_e32 v21, 0xc01d265f, v20
	v_exp_f32_e32 v21, v21
	global_store_dword v[16:17], v23, off
	v_add_f32_e32 v23, v91, v7
	v_min_f32_e32 v23, 0x40e00000, v23
	v_add_f32_e32 v21, 1.0, v21
	v_mul_f32_e32 v24, 0xc01d265f, v23
	v_rcp_f32_e32 v21, v21
	v_exp_f32_e32 v24, v24
	v_add_f32_e32 v22, v58, v2
	v_mul_f32_e32 v20, v20, v21
	v_med3_f32 v21, v22, s80, v206
	v_mul_f32_e32 v20, v21, v20
	v_add_f32_e32 v21, 1.0, v24
	v_rcp_f32_e32 v21, v21
	v_add_f32_e32 v22, v59, v3
	v_mul_f32_e32 v21, v23, v21
	v_mov_b32_e32 v23, v183
	v_cvt_pk_fp8_f32 v23, v18, v19
	v_med3_f32 v18, v22, s80, v206
	v_mul_f32_e32 v18, v18, v21
	v_add_f32_e32 v8, v84, v8
	v_min_f32_e32 v8, 0x40e00000, v8
	v_cvt_pk_fp8_f32 v23, v20, v18 op_sel:[0,0,1]
	v_mul_f32_e32 v18, 0xc01d265f, v8
	v_exp_f32_e32 v18, v18
	v_add_f32_e32 v9, v85, v9
	v_min_f32_e32 v9, 0x40e00000, v9
	v_mul_f32_e32 v19, 0xc01d265f, v9
	v_add_f32_e32 v18, 1.0, v18
	v_rcp_f32_e32 v18, v18
	v_exp_f32_e32 v19, v19
	v_add_f32_e32 v12, v52, v12
	v_med3_f32 v12, v12, s80, v206
	v_mul_f32_e32 v8, v8, v18
	v_mul_f32_e32 v8, v12, v8
	v_add_f32_e32 v12, 1.0, v19
	v_rcp_f32_e32 v12, v12
	v_add_f32_e32 v13, v53, v13
	v_add_f32_e32 v10, v86, v10
	v_mul_f32_e32 v9, v9, v12
	v_med3_f32 v12, v13, s80, v206
	v_min_f32_e32 v10, 0x40e00000, v10
	v_mul_f32_e32 v9, v12, v9
	v_mul_f32_e32 v12, 0xc01d265f, v10
	v_exp_f32_e32 v12, v12
	v_add_f32_e32 v11, v87, v11
	v_min_f32_e32 v11, 0x40e00000, v11
	v_add_f32_e32 v13, v54, v14
	v_add_f32_e32 v12, 1.0, v12
	v_mul_f32_e32 v14, 0xc01d265f, v11
	v_rcp_f32_e32 v12, v12
	v_exp_f32_e32 v14, v14
	v_mul_f32_e32 v10, v10, v12
	v_med3_f32 v12, v13, s80, v206
	v_mul_f32_e32 v10, v12, v10
	v_add_f32_e32 v12, 1.0, v14
	v_rcp_f32_e32 v12, v12
	v_add_f32_e32 v13, v55, v15
	v_mul_f32_e32 v11, v11, v12
	v_mov_b32_e32 v12, v183
	v_cvt_pk_fp8_f32 v12, v8, v9
	v_med3_f32 v8, v13, s80, v206
	v_mul_f32_e32 v8, v8, v11
	v_add_f32_e32 v4, v80, v4
	v_min_f32_e32 v4, 0x40e00000, v4
	v_cvt_pk_fp8_f32 v12, v10, v8 op_sel:[0,0,1]
	v_mul_f32_e32 v8, 0xc01d265f, v4
	v_exp_f32_e32 v8, v8
	v_add_f32_e32 v5, v81, v5
	v_min_f32_e32 v5, 0x40e00000, v5
	v_mul_f32_e32 v9, 0xc01d265f, v5
	v_add_f32_e32 v8, 1.0, v8
	v_rcp_f32_e32 v8, v8
	v_exp_f32_e32 v9, v9
	v_add_f32_e32 v0, v48, v0
	v_med3_f32 v0, v0, s80, v206
	v_mul_f32_e32 v4, v4, v8
	v_mul_f32_e32 v0, v0, v4
	v_add_f32_e32 v4, 1.0, v9
	v_rcp_f32_e32 v4, v4
	v_add_f32_e32 v1, v49, v1
	v_med3_f32 v1, v1, s80, v206
	v_mul_f32_e32 v4, v5, v4
	v_mul_f32_e32 v1, v1, v4
	v_add_f32_e32 v4, v82, v6
	v_min_f32_e32 v4, 0x40e00000, v4
	v_mul_f32_e32 v5, 0xc01d265f, v4
	v_exp_f32_e32 v5, v5
	v_add_f32_e32 v6, v83, v7
	v_min_f32_e32 v6, 0x40e00000, v6
	v_mul_f32_e32 v7, 0xc01d265f, v6
	v_add_f32_e32 v5, 1.0, v5
	v_rcp_f32_e32 v5, v5
	v_exp_f32_e32 v7, v7
	v_add_f32_e32 v2, v50, v2
	v_med3_f32 v2, v2, s80, v206
	v_mul_f32_e32 v4, v4, v5
	v_mul_f32_e32 v2, v2, v4
	v_add_f32_e32 v4, 1.0, v7
	v_rcp_f32_e32 v4, v4
	v_add_f32_e32 v3, v51, v3
	v_mov_b32_e32 v5, v183
	v_cvt_pk_fp8_f32 v5, v0, v1
	v_mul_f32_e32 v4, v6, v4
	v_med3_f32 v0, v3, s80, v206
	v_mul_f32_e32 v0, v0, v4
	v_cvt_pk_fp8_f32 v5, v2, v0 op_sel:[0,0,1]
	s_andn2_b64 vcc, exec, s[24:25]
	global_store_dword v[16:17], v23, off offset:16
	global_store_dword v[16:17], v12, off offset:2048
	global_store_dword v[16:17], v5, off offset:2064
	s_cbranch_vccnz .LBB0_784
	v_mov_b32_e32 v48, 0
	s_mov_b32 s71, s44
	s_mov_b32 s8, s22
	s_mov_b64 s[6:7], s[20:21]
	s_mov_b32 s4, s18
	s_mov_b32 s45, s72
	s_mov_b32 s10, s19
	s_mov_b32 s76, s52
	v_mov_b32_e32 v49, v48
	v_mov_b32_e32 v50, v48
	v_mov_b32_e32 v51, v48
	v_mov_b32_e32 v52, v48
	v_mov_b32_e32 v53, v48
	v_mov_b32_e32 v54, v48
	v_mov_b32_e32 v55, v48
	v_mov_b32_e32 v56, v48
	v_mov_b32_e32 v57, v48
	v_mov_b32_e32 v58, v48
	v_mov_b32_e32 v59, v48
	v_mov_b32_e32 v60, v48
	v_mov_b32_e32 v61, v48
	v_mov_b32_e32 v62, v48
	v_mov_b32_e32 v63, v48
	v_mov_b32_e32 v64, v48
	v_mov_b32_e32 v65, v48
	v_mov_b32_e32 v66, v48
	v_mov_b32_e32 v67, v48
	v_mov_b32_e32 v68, v48
	v_mov_b32_e32 v69, v48
	v_mov_b32_e32 v70, v48
	v_mov_b32_e32 v71, v48
	v_mov_b32_e32 v72, v48
	v_mov_b32_e32 v73, v48
	v_mov_b32_e32 v74, v48
	v_mov_b32_e32 v75, v48
	v_mov_b32_e32 v76, v48
	v_mov_b32_e32 v77, v48
	v_mov_b32_e32 v78, v48
	v_mov_b32_e32 v79, v48
	v_mov_b32_e32 v80, v48
	v_mov_b32_e32 v81, v48
	v_mov_b32_e32 v82, v48
	v_mov_b32_e32 v83, v48
	v_mov_b32_e32 v84, v48
	v_mov_b32_e32 v85, v48
	v_mov_b32_e32 v86, v48
	v_mov_b32_e32 v87, v48
	v_mov_b32_e32 v88, v48
	v_mov_b32_e32 v89, v48
	v_mov_b32_e32 v90, v48
	v_mov_b32_e32 v91, v48
	v_mov_b32_e32 v92, v48
	v_mov_b32_e32 v93, v48
	v_mov_b32_e32 v94, v48
	v_mov_b32_e32 v95, v48
	v_mov_b32_e32 v96, v48
	v_mov_b32_e32 v97, v48
	v_mov_b32_e32 v98, v48
	v_mov_b32_e32 v99, v48
	v_mov_b32_e32 v100, v48
	v_mov_b32_e32 v101, v48
	v_mov_b32_e32 v102, v48
	v_mov_b32_e32 v103, v48
	v_mov_b32_e32 v104, v48
	v_mov_b32_e32 v105, v48
	v_mov_b32_e32 v106, v48
	v_mov_b32_e32 v107, v48
	v_mov_b32_e32 v108, v48
	v_mov_b32_e32 v109, v48
	v_mov_b32_e32 v110, v48
	v_mov_b32_e32 v111, v48
	v_mov_b32_e32 v112, v48
	v_mov_b32_e32 v113, v48
	v_mov_b32_e32 v114, v48
	v_mov_b32_e32 v115, v48
	v_mov_b32_e32 v116, v48
	v_mov_b32_e32 v117, v48
	v_mov_b32_e32 v118, v48
	v_mov_b32_e32 v119, v48
	v_mov_b32_e32 v120, v48
	v_mov_b32_e32 v121, v48
	v_mov_b32_e32 v122, v48
	v_mov_b32_e32 v123, v48
	v_mov_b32_e32 v124, v48
	v_mov_b32_e32 v125, v48
	v_mov_b32_e32 v126, v48
	v_mov_b32_e32 v127, v48
	v_mov_b32_e32 v128, v48
	v_mov_b32_e32 v129, v48
	v_mov_b32_e32 v130, v48
	v_mov_b32_e32 v131, v48
	v_mov_b32_e32 v132, v48
	v_mov_b32_e32 v133, v48
	v_mov_b32_e32 v134, v48
	v_mov_b32_e32 v135, v48
	v_mov_b32_e32 v136, v48
	v_mov_b32_e32 v137, v48
	v_mov_b32_e32 v138, v48
	v_mov_b32_e32 v139, v48
	v_mov_b32_e32 v140, v48
	v_mov_b32_e32 v141, v48
	v_mov_b32_e32 v142, v48
	v_mov_b32_e32 v143, v48
	v_mov_b32_e32 v144, v48
	v_mov_b32_e32 v145, v48
	v_mov_b32_e32 v146, v48
	v_mov_b32_e32 v147, v48
	v_mov_b32_e32 v148, v48
	v_mov_b32_e32 v149, v48
	v_mov_b32_e32 v150, v48
	v_mov_b32_e32 v151, v48
	v_mov_b32_e32 v152, v48
	v_mov_b32_e32 v153, v48
	v_mov_b32_e32 v154, v48
	v_mov_b32_e32 v155, v48
	v_mov_b32_e32 v156, v48
	v_mov_b32_e32 v157, v48
	v_mov_b32_e32 v158, v48
	v_mov_b32_e32 v159, v48
	v_mov_b32_e32 v160, v48
	v_mov_b32_e32 v161, v48
	v_mov_b32_e32 v162, v48
	v_mov_b32_e32 v163, v48
	v_mov_b32_e32 v164, v48
	v_mov_b32_e32 v165, v48
	v_mov_b32_e32 v166, v48
	v_mov_b32_e32 v167, v48
	v_mov_b32_e32 v168, v48
	v_mov_b32_e32 v169, v48
	v_mov_b32_e32 v170, v48
	v_mov_b32_e32 v171, v48
	v_mov_b32_e32 v172, v48
	v_mov_b32_e32 v173, v48
	v_mov_b32_e32 v174, v48
	v_mov_b32_e32 v175, v48
	s_branch .LBB0_784
